# P7 down-GEMM epilogue: the 8 serial gate loads and 4 bias/scale loads issued as one batch; stacked on v022
# speedup vs baseline: 1.0033x; 1.0033x over previous
.LBB0_590:
	s_lshl_b32 s1, s40, 2
	s_add_i32 s1, s1, 0
	s_nop 15
	s_nop 15
	s_add_i32 s1, s1, 0x20480
	v_mov_b32_e32 v2, s1
	ds_read_b32 v2, v2
	s_ashr_i32 s41, s40, 31
	s_lshl_b64 s[18:19], s[40:41], 18
	s_add_u32 s18, s78, s18
	s_addc_u32 s19, s79, s19
	s_waitcnt lgkmcnt(0)
	v_sub_u32_e32 v2, s26, v2
	v_lshl_add_u32 v2, v2, 8, v1
	v_ashrrev_i32_e32 v3, 31, v2
	v_lshl_add_u64 v[2:3], v[2:3], 2, s[18:19]
	global_load_dword v28, v[2:3], off
	global_load_dword v26, v[2:3], off offset:64
	global_load_dword v24, v[2:3], off offset:128
	global_load_dword v22, v[2:3], off offset:192
	global_load_dword v20, v[2:3], off offset:512
	global_load_dword v18, v[2:3], off offset:576
	global_load_dword v16, v[2:3], off offset:640
	global_load_dword v14, v[2:3], off offset:704
	v_readlane_b32 s84, v252, 0
	v_readlane_b32 s88, v252, 4
	v_readlane_b32 s89, v252, 5
	s_lshl_b64 s[18:19], s[40:41], 12
	v_readlane_b32 s90, v252, 6
	v_readlane_b32 s91, v252, 7
	s_mov_b64 s[40:41], s[88:89]
	s_add_u32 s22, s40, s18
	s_addc_u32 s23, s41, s19
	s_add_u32 s18, s48, s18
	s_addc_u32 s19, s49, s19
	v_lshl_add_u32 v15, s26, 8, v1
	s_andn2_b64 vcc, exec, s[14:15]
	v_readlane_b32 s85, v252, 1
	v_readlane_b32 s86, v252, 2
	v_readlane_b32 s87, v252, 3
	s_mov_b64 s[42:43], s[90:91]
	v_lshl_or_b32 v2, s28, 8, v209
	v_ashrrev_i32_e32 v3, 31, v2
	v_sub_u32_e32 v30, v2, v190
	v_lshlrev_b64 v[2:3], 2, v[2:3]
	v_lshl_add_u64 v[180:181], s[22:23], 0, v[2:3]
	v_lshl_add_u64 v[32:33], s[18:19], 0, v[2:3]
	global_load_dwordx4 v[2:5], v[180:181], off offset:16
	global_load_dwordx4 v[6:9], v[180:181], off
	global_load_dwordx4 v[10:13], v[32:33], off offset:16
	global_load_dwordx4 v[182:185], v[32:33], off
	s_waitcnt vmcnt(0)
	v_mul_f32_e32 v28, 4.0, v28
	v_mul_f32_e32 v26, 4.0, v26
	v_mul_f32_e32 v24, 4.0, v24
	v_mul_f32_e32 v22, 4.0, v22
	v_mul_f32_e32 v20, 4.0, v20
	v_mul_f32_e32 v18, 4.0, v18
	v_mul_f32_e32 v16, 4.0, v16
	v_mul_f32_e32 v14, 4.0, v14
	v_ashrrev_i32_e32 v31, 31, v30
	s_mov_b64 s[18:19], -1
	s_waitcnt vmcnt(0)
	v_pk_mul_f32 v[186:187], v[184:185], s[8:9] op_sel_hi:[1,0]
	v_pk_mul_f32 v[188:189], v[182:183], s[8:9] op_sel_hi:[1,0]
	v_pk_mul_f32 v[182:183], v[12:13], s[8:9] op_sel_hi:[1,0]
	v_pk_mul_f32 v[184:185], v[10:11], s[8:9] op_sel_hi:[1,0]
	v_pk_fma_f32 v[10:11], v[160:161], v[186:187], v[8:9]
	v_pk_fma_f32 v[12:13], v[158:159], v[188:189], v[6:7]
	v_pk_mul_f32 v[158:159], v[28:29], v[10:11] op_sel_hi:[0,1]
	v_pk_mul_f32 v[12:13], v[28:29], v[12:13] op_sel_hi:[0,1]
	v_pk_fma_f32 v[10:11], v[156:157], v[182:183], v[4:5]
	v_pk_fma_f32 v[154:155], v[154:155], v[184:185], v[2:3]
	v_pk_mul_f32 v[156:157], v[28:29], v[10:11] op_sel_hi:[0,1]
	v_med3_f32 v11, v12, s56, v212
	v_med3_f32 v12, v13, s56, v212
	v_mov_b32_e32 v10, 0
	v_cvt_pk_fp8_f32 v10, v11, v12
	v_pk_mul_f32 v[154:155], v[28:29], v[154:155] op_sel_hi:[0,1]
	v_med3_f32 v11, v158, s56, v212
	v_med3_f32 v12, v159, s56, v212
	v_cvt_pk_fp8_f32 v10, v11, v12 op_sel:[0,0,1]
	v_med3_f32 v12, v154, s56, v212
	v_med3_f32 v13, v155, s56, v212
	v_mov_b32_e32 v11, 0
	v_cvt_pk_fp8_f32 v11, v12, v13
	v_med3_f32 v12, v156, s56, v212
	v_med3_f32 v13, v157, s56, v212
	v_pk_fma_f32 v[150:151], v[150:151], v[188:189], v[6:7]
	v_cvt_pk_fp8_f32 v11, v12, v13 op_sel:[0,0,1]
	v_pk_fma_f32 v[12:13], v[152:153], v[186:187], v[8:9]
	v_pk_mul_f32 v[150:151], v[26:27], v[150:151] op_sel_hi:[0,1]
	v_pk_mul_f32 v[152:153], v[26:27], v[12:13] op_sel_hi:[0,1]
	v_pk_fma_f32 v[12:13], v[148:149], v[182:183], v[4:5]
	v_med3_f32 v17, v151, s56, v212
	v_pk_mul_f32 v[148:149], v[26:27], v[12:13] op_sel_hi:[0,1]
	v_med3_f32 v13, v150, s56, v212
	v_mov_b32_e32 v12, 0
	v_cvt_pk_fp8_f32 v12, v13, v17
	v_pk_fma_f32 v[146:147], v[146:147], v[184:185], v[2:3]
	v_med3_f32 v13, v152, s56, v212
	v_pk_mul_f32 v[146:147], v[26:27], v[146:147] op_sel_hi:[0,1]
	v_med3_f32 v17, v153, s56, v212
	v_cvt_pk_fp8_f32 v12, v13, v17 op_sel:[0,0,1]
	v_med3_f32 v17, v146, s56, v212
	v_med3_f32 v19, v147, s56, v212
	v_mov_b32_e32 v13, 0
	v_cvt_pk_fp8_f32 v13, v17, v19
	v_med3_f32 v17, v148, s56, v212
	v_med3_f32 v19, v149, s56, v212
	v_or_b32_e32 v146, v15, v191
	v_cvt_pk_fp8_f32 v13, v17, v19 op_sel:[0,0,1]
	v_ashrrev_i32_e32 v147, 31, v146
	v_lshlrev_b64 v[146:147], 10, v[146:147]
	v_lshl_add_u64 v[146:147], s[92:93], 0, v[146:147]
	v_permlane16_swap_b32_e32 v10, v12
	v_permlane16_swap_b32_e32 v11, v13
	v_lshl_add_u64 v[146:147], v[146:147], 0, v[30:31]
	global_store_dwordx4 v[146:147], v[10:13], off
	v_pk_fma_f32 v[138:139], v[138:139], v[184:185], v[2:3]
	v_pk_fma_f32 v[140:141], v[140:141], v[182:183], v[4:5]
	v_pk_fma_f32 v[12:13], v[142:143], v[188:189], v[6:7]
	v_pk_mul_f32 v[142:143], v[24:25], v[138:139] op_sel_hi:[0,1]
	v_pk_mul_f32 v[12:13], v[24:25], v[12:13] op_sel_hi:[0,1]
	v_med3_f32 v12, v12, s56, v212
	v_med3_f32 v13, v13, s56, v212
	v_mov_b32_e32 v138, 0
	v_cvt_pk_fp8_f32 v138, v12, v13
	v_pk_fma_f32 v[10:11], v[144:145], v[186:187], v[8:9]
	v_pk_fma_f32 v[12:13], v[134:135], v[188:189], v[6:7]
	v_pk_mul_f32 v[10:11], v[24:25], v[10:11] op_sel_hi:[0,1]
	v_med3_f32 v10, v10, s56, v212
	v_med3_f32 v11, v11, s56, v212
	v_pk_mul_f32 v[140:141], v[24:25], v[140:141] op_sel_hi:[0,1]
	v_cvt_pk_fp8_f32 v138, v10, v11 op_sel:[0,0,1]
	v_med3_f32 v10, v142, s56, v212
	v_med3_f32 v11, v143, s56, v212
	v_mov_b32_e32 v139, 0
	v_pk_mul_f32 v[12:13], v[22:23], v[12:13] op_sel_hi:[0,1]
	v_pk_fma_f32 v[126:127], v[126:127], v[188:189], v[6:7]
	v_cvt_pk_fp8_f32 v139, v10, v11
	v_med3_f32 v10, v140, s56, v212
	v_med3_f32 v12, v12, s56, v212
	v_med3_f32 v13, v13, s56, v212
	v_mov_b32_e32 v140, 0
	v_pk_mul_f32 v[126:127], v[20:21], v[126:127] op_sel_hi:[0,1]
	v_pk_fma_f32 v[122:123], v[122:123], v[184:185], v[2:3]
	v_cvt_pk_fp8_f32 v140, v12, v13
	v_pk_fma_f32 v[12:13], v[128:129], v[186:187], v[8:9]
	v_pk_mul_f32 v[128:129], v[20:21], v[122:123] op_sel_hi:[0,1]
	v_med3_f32 v17, v126, s56, v212
	v_med3_f32 v19, v127, s56, v212
	v_mov_b32_e32 v122, 0
	v_cvt_pk_fp8_f32 v122, v17, v19
	v_pk_mul_f32 v[12:13], v[20:21], v[12:13] op_sel_hi:[0,1]
	v_med3_f32 v12, v12, s56, v212
	v_med3_f32 v13, v13, s56, v212
	v_cvt_pk_fp8_f32 v122, v12, v13 op_sel:[0,0,1]
	v_med3_f32 v12, v128, s56, v212
	v_med3_f32 v13, v129, s56, v212
	v_mov_b32_e32 v123, 0
	v_cvt_pk_fp8_f32 v123, v12, v13
	v_pk_fma_f32 v[124:125], v[124:125], v[182:183], v[4:5]
	v_pk_fma_f32 v[118:119], v[118:119], v[188:189], v[6:7]
	v_pk_mul_f32 v[124:125], v[20:21], v[124:125] op_sel_hi:[0,1]
	v_med3_f32 v12, v124, s56, v212
	v_med3_f32 v13, v125, s56, v212
	v_cvt_pk_fp8_f32 v123, v12, v13 op_sel:[0,0,1]
	v_pk_fma_f32 v[12:13], v[120:121], v[186:187], v[8:9]
	v_pk_mul_f32 v[118:119], v[18:19], v[118:119] op_sel_hi:[0,1]
	v_pk_fma_f32 v[116:117], v[116:117], v[182:183], v[4:5]
	v_pk_fma_f32 v[114:115], v[114:115], v[184:185], v[2:3]
	v_med3_f32 v11, v141, s56, v212
	v_pk_mul_f32 v[12:13], v[18:19], v[12:13] op_sel_hi:[0,1]
	v_pk_mul_f32 v[114:115], v[18:19], v[114:115] op_sel_hi:[0,1]
	v_pk_mul_f32 v[116:117], v[18:19], v[116:117] op_sel_hi:[0,1]
	v_med3_f32 v17, v118, s56, v212
	v_med3_f32 v19, v119, s56, v212
	v_mov_b32_e32 v124, 0
	v_cvt_pk_fp8_f32 v139, v10, v11 op_sel:[0,0,1]
	v_pk_fma_f32 v[10:11], v[136:137], v[186:187], v[8:9]
	v_cvt_pk_fp8_f32 v124, v17, v19
	v_pk_mul_f32 v[10:11], v[22:23], v[10:11] op_sel_hi:[0,1]
	v_pk_fma_f32 v[130:131], v[130:131], v[184:185], v[2:3]
	v_med3_f32 v10, v10, s56, v212
	v_pk_mul_f32 v[130:131], v[22:23], v[130:131] op_sel_hi:[0,1]
	v_med3_f32 v11, v11, s56, v212
	v_pk_fma_f32 v[110:111], v[110:111], v[188:189], v[6:7]
	v_cvt_pk_fp8_f32 v140, v10, v11 op_sel:[0,0,1]
	v_med3_f32 v10, v130, s56, v212
	v_med3_f32 v11, v131, s56, v212
	v_mov_b32_e32 v141, 0
	v_med3_f32 v12, v12, s56, v212
	v_med3_f32 v13, v13, s56, v212
	v_pk_fma_f32 v[112:113], v[112:113], v[186:187], v[8:9]
	v_pk_mul_f32 v[110:111], v[16:17], v[110:111] op_sel_hi:[0,1]
	v_pk_fma_f32 v[108:109], v[108:109], v[182:183], v[4:5]
	v_pk_fma_f32 v[106:107], v[106:107], v[184:185], v[2:3]
	v_cvt_pk_fp8_f32 v141, v10, v11
	v_cvt_pk_fp8_f32 v124, v12, v13 op_sel:[0,0,1]
	v_med3_f32 v12, v114, s56, v212
	v_med3_f32 v13, v115, s56, v212
	v_pk_mul_f32 v[112:113], v[16:17], v[112:113] op_sel_hi:[0,1]
	v_pk_mul_f32 v[114:115], v[16:17], v[106:107] op_sel_hi:[0,1]
	v_pk_mul_f32 v[108:109], v[16:17], v[108:109] op_sel_hi:[0,1]
	v_med3_f32 v17, v110, s56, v212
	v_med3_f32 v19, v111, s56, v212
	v_mov_b32_e32 v106, 0
	v_pk_fma_f32 v[132:133], v[132:133], v[182:183], v[4:5]
	v_cvt_pk_fp8_f32 v106, v17, v19
	v_pk_mul_f32 v[132:133], v[22:23], v[132:133] op_sel_hi:[0,1]
	v_med3_f32 v10, v132, s56, v212
	v_med3_f32 v11, v133, s56, v212
	v_cvt_pk_fp8_f32 v141, v10, v11 op_sel:[0,0,1]
	v_or_b32_e32 v10, v15, v192
	v_add_u32_e32 v15, 0x80, v15
	v_med3_f32 v17, v112, s56, v212
	v_med3_f32 v19, v113, s56, v212
	v_pk_fma_f32 v[6:7], v[102:103], v[188:189], v[6:7]
	v_pk_fma_f32 v[2:3], v[98:99], v[184:185], v[2:3]
	v_cvt_pk_fp8_f32 v106, v17, v19 op_sel:[0,0,1]
	v_med3_f32 v17, v114, s56, v212
	v_med3_f32 v19, v115, s56, v212
	v_mov_b32_e32 v107, 0
	v_pk_mul_f32 v[6:7], v[14:15], v[6:7] op_sel_hi:[0,1]
	v_pk_mul_f32 v[2:3], v[14:15], v[2:3] op_sel_hi:[0,1]
	v_mov_b32_e32 v125, 0
	v_cvt_pk_fp8_f32 v107, v17, v19
	v_med3_f32 v17, v108, s56, v212
	v_med3_f32 v19, v109, s56, v212
	v_med3_f32 v6, v6, s56, v212
	v_med3_f32 v7, v7, s56, v212
	v_mov_b32_e32 v108, 0
	v_med3_f32 v2, v2, s56, v212
	v_med3_f32 v3, v3, s56, v212
	v_mov_b32_e32 v109, 0
	v_cvt_pk_fp8_f32 v125, v12, v13
	v_cvt_pk_fp8_f32 v108, v6, v7
	v_cvt_pk_fp8_f32 v109, v2, v3
	v_pk_fma_f32 v[8:9], v[104:105], v[186:187], v[8:9]
	v_pk_fma_f32 v[4:5], v[100:101], v[182:183], v[4:5]
	v_pk_mul_f32 v[8:9], v[14:15], v[8:9] op_sel_hi:[0,1]
	v_pk_mul_f32 v[4:5], v[14:15], v[4:5] op_sel_hi:[0,1]
	v_med3_f32 v12, v116, s56, v212
	v_med3_f32 v13, v117, s56, v212
	v_med3_f32 v6, v8, s56, v212
	v_med3_f32 v7, v9, s56, v212
	v_med3_f32 v2, v4, s56, v212
	v_med3_f32 v3, v5, s56, v212
	v_cvt_pk_fp8_f32 v125, v12, v13 op_sel:[0,0,1]
	v_or_b32_e32 v12, v15, v191
	v_cvt_pk_fp8_f32 v107, v17, v19 op_sel:[0,0,1]
	v_cvt_pk_fp8_f32 v108, v6, v7 op_sel:[0,0,1]
	v_cvt_pk_fp8_f32 v109, v2, v3 op_sel:[0,0,1]
	v_or_b32_e32 v2, v15, v192
	v_ashrrev_i32_e32 v11, 31, v10
	v_ashrrev_i32_e32 v13, 31, v12
	v_ashrrev_i32_e32 v3, 31, v2
	v_lshlrev_b64 v[10:11], 10, v[10:11]
	v_lshlrev_b64 v[12:13], 10, v[12:13]
	v_lshlrev_b64 v[2:3], 10, v[2:3]
	v_lshl_add_u64 v[10:11], s[92:93], 0, v[10:11]
	v_lshl_add_u64 v[12:13], s[92:93], 0, v[12:13]
	v_lshl_add_u64 v[2:3], s[92:93], 0, v[2:3]
	v_permlane16_swap_b32_e32 v138, v140
	v_permlane16_swap_b32_e32 v139, v141
	v_lshl_add_u64 v[10:11], v[10:11], 0, v[30:31]
	v_permlane16_swap_b32_e32 v122, v124
	v_permlane16_swap_b32_e32 v123, v125
	v_lshl_add_u64 v[12:13], v[12:13], 0, v[30:31]
	v_permlane16_swap_b32_e32 v106, v108
	v_permlane16_swap_b32_e32 v107, v109
	v_lshl_add_u64 v[30:31], v[2:3], 0, v[30:31]
	global_store_dwordx4 v[10:11], v[138:141], off
	global_store_dwordx4 v[12:13], v[122:125], off
	global_store_dwordx4 v[30:31], v[106:109], off
	global_load_dwordx4 v[2:5], v[180:181], off offset:528
	global_load_dwordx4 v[6:9], v[180:181], off offset:512
	s_nop 0
	global_load_dwordx4 v[104:107], v[32:33], off offset:528
	global_load_dwordx4 v[98:101], v[32:33], off offset:512
	s_waitcnt vmcnt(1)
	v_pk_mul_f32 v[32:33], v[106:107], s[8:9] op_sel_hi:[1,0]
	s_waitcnt vmcnt(0)
	v_pk_mul_f32 v[102:103], v[98:99], s[8:9] op_sel_hi:[1,0]
	v_pk_mul_f32 v[98:99], v[104:105], s[8:9] op_sel_hi:[1,0]
	v_pk_fma_f32 v[94:95], v[94:95], v[102:103], v[6:7]
	v_pk_fma_f32 v[90:91], v[90:91], v[98:99], v[2:3]
	v_pk_mul_f32 v[94:95], v[28:29], v[94:95] op_sel_hi:[0,1]
	v_pk_mul_f32 v[104:105], v[28:29], v[90:91] op_sel_hi:[0,1]
	v_med3_f32 v15, v94, s56, v212
	v_med3_f32 v17, v95, s56, v212
	v_mov_b32_e32 v90, 0
	v_pk_mul_f32 v[100:101], v[100:101], s[8:9] op_sel_hi:[1,0]
	v_cvt_pk_fp8_f32 v90, v15, v17
	v_pk_fma_f32 v[96:97], v[96:97], v[100:101], v[8:9]
	v_mov_b32_e32 v91, 0
	v_pk_mul_f32 v[96:97], v[28:29], v[96:97] op_sel_hi:[0,1]
	v_med3_f32 v15, v96, s56, v212
	v_med3_f32 v17, v97, s56, v212
	v_cvt_pk_fp8_f32 v90, v15, v17 op_sel:[0,0,1]
	v_med3_f32 v15, v104, s56, v212
	v_med3_f32 v17, v105, s56, v212
	v_cvt_pk_fp8_f32 v91, v15, v17
	v_pk_fma_f32 v[92:93], v[92:93], v[32:33], v[4:5]
	v_pk_fma_f32 v[86:87], v[86:87], v[102:103], v[6:7]
	v_pk_mul_f32 v[28:29], v[28:29], v[92:93] op_sel_hi:[0,1]
	v_med3_f32 v15, v28, s56, v212
	v_med3_f32 v17, v29, s56, v212
	v_pk_mul_f32 v[86:87], v[26:27], v[86:87] op_sel_hi:[0,1]
	v_cvt_pk_fp8_f32 v91, v15, v17 op_sel:[0,0,1]
	v_med3_f32 v15, v86, s56, v212
	v_med3_f32 v17, v87, s56, v212
	v_mov_b32_e32 v92, 0
	v_cvt_pk_fp8_f32 v92, v15, v17
	v_pk_fma_f32 v[28:29], v[88:89], v[100:101], v[8:9]
	v_pk_fma_f32 v[82:83], v[82:83], v[98:99], v[2:3]
	v_pk_mul_f32 v[28:29], v[26:27], v[28:29] op_sel_hi:[0,1]
	v_pk_mul_f32 v[82:83], v[26:27], v[82:83] op_sel_hi:[0,1]
	v_med3_f32 v15, v28, s56, v212
	v_med3_f32 v17, v29, s56, v212
	v_cvt_pk_fp8_f32 v92, v15, v17 op_sel:[0,0,1]
	v_med3_f32 v15, v82, s56, v212
	v_med3_f32 v17, v83, s56, v212
	v_mov_b32_e32 v93, 0
	v_cvt_pk_fp8_f32 v93, v15, v17
	v_pk_fma_f32 v[84:85], v[84:85], v[32:33], v[4:5]
	v_pk_fma_f32 v[28:29], v[78:79], v[102:103], v[6:7]
	v_pk_mul_f32 v[26:27], v[26:27], v[84:85] op_sel_hi:[0,1]
	v_med3_f32 v15, v26, s56, v212
	v_med3_f32 v17, v27, s56, v212
	v_pk_fma_f32 v[26:27], v[80:81], v[100:101], v[8:9]
	v_pk_mul_f32 v[28:29], v[24:25], v[28:29] op_sel_hi:[0,1]
	v_pk_fma_f32 v[76:77], v[76:77], v[32:33], v[4:5]
	v_pk_fma_f32 v[74:75], v[74:75], v[98:99], v[2:3]
	v_cvt_pk_fp8_f32 v93, v15, v17 op_sel:[0,0,1]
	v_pk_mul_f32 v[26:27], v[24:25], v[26:27] op_sel_hi:[0,1]
	v_pk_mul_f32 v[74:75], v[24:25], v[74:75] op_sel_hi:[0,1]
	v_pk_mul_f32 v[76:77], v[24:25], v[76:77] op_sel_hi:[0,1]
	v_med3_f32 v15, v28, s56, v212
	v_med3_f32 v17, v29, s56, v212
	v_mov_b32_e32 v24, 0
	v_cvt_pk_fp8_f32 v24, v15, v17
	v_med3_f32 v15, v26, s56, v212
	v_med3_f32 v17, v27, s56, v212
	v_mov_b32_e32 v25, 0
	v_cvt_pk_fp8_f32 v24, v15, v17 op_sel:[0,0,1]
	v_med3_f32 v15, v74, s56, v212
	v_med3_f32 v17, v75, s56, v212
	v_cvt_pk_fp8_f32 v25, v15, v17
	v_pk_fma_f32 v[26:27], v[64:65], v[100:101], v[8:9]
	v_pk_fma_f32 v[28:29], v[62:63], v[102:103], v[6:7]
	v_med3_f32 v15, v76, s56, v212
	v_med3_f32 v17, v77, s56, v212
	v_pk_mul_f32 v[28:29], v[22:23], v[28:29] op_sel_hi:[0,1]
	v_pk_mul_f32 v[62:63], v[22:23], v[26:27] op_sel_hi:[0,1]
	v_pk_fma_f32 v[26:27], v[60:61], v[32:33], v[4:5]
	v_pk_fma_f32 v[58:59], v[58:59], v[98:99], v[2:3]
	v_cvt_pk_fp8_f32 v25, v15, v17 op_sel:[0,0,1]
	v_pk_mul_f32 v[58:59], v[22:23], v[58:59] op_sel_hi:[0,1]
	v_pk_mul_f32 v[22:23], v[22:23], v[26:27] op_sel_hi:[0,1]
	v_med3_f32 v15, v28, s56, v212
	v_med3_f32 v17, v29, s56, v212
	v_mov_b32_e32 v26, 0
	v_cvt_pk_fp8_f32 v26, v15, v17
	v_med3_f32 v15, v62, s56, v212
	v_med3_f32 v17, v63, s56, v212
	v_mov_b32_e32 v27, 0
	v_cvt_pk_fp8_f32 v26, v15, v17 op_sel:[0,0,1]
	v_med3_f32 v15, v58, s56, v212
	v_med3_f32 v17, v59, s56, v212
	v_cvt_pk_fp8_f32 v27, v15, v17
	v_med3_f32 v15, v22, s56, v212
	v_med3_f32 v17, v23, s56, v212
	v_permlane16_swap_b32_e32 v24, v26
	v_cvt_pk_fp8_f32 v27, v15, v17 op_sel:[0,0,1]
	v_pk_fma_f32 v[22:23], v[70:71], v[102:103], v[6:7]
	v_permlane16_swap_b32_e32 v90, v92
	v_permlane16_swap_b32_e32 v25, v27
	global_store_dwordx4 v[10:11], v[24:27], off offset:128
	v_pk_fma_f32 v[10:11], v[72:73], v[100:101], v[8:9]
	v_pk_mul_f32 v[22:23], v[20:21], v[22:23] op_sel_hi:[0,1]
	v_pk_fma_f32 v[24:25], v[68:69], v[32:33], v[4:5]
	v_pk_fma_f32 v[26:27], v[66:67], v[98:99], v[2:3]
	v_pk_mul_f32 v[10:11], v[20:21], v[10:11] op_sel_hi:[0,1]
	v_pk_mul_f32 v[26:27], v[20:21], v[26:27] op_sel_hi:[0,1]
	v_pk_mul_f32 v[24:25], v[20:21], v[24:25] op_sel_hi:[0,1]
	v_med3_f32 v15, v22, s56, v212
	v_med3_f32 v17, v23, s56, v212
	v_mov_b32_e32 v20, 0
	v_cvt_pk_fp8_f32 v20, v15, v17
	v_med3_f32 v10, v10, s56, v212
	v_med3_f32 v11, v11, s56, v212
	v_mov_b32_e32 v21, 0
	v_cvt_pk_fp8_f32 v20, v10, v11 op_sel:[0,0,1]
	v_med3_f32 v10, v26, s56, v212
	v_med3_f32 v11, v27, s56, v212
	v_cvt_pk_fp8_f32 v21, v10, v11
	v_pk_fma_f32 v[22:23], v[54:55], v[102:103], v[6:7]
	v_med3_f32 v10, v24, s56, v212
	v_pk_mul_f32 v[22:23], v[18:19], v[22:23] op_sel_hi:[0,1]
	v_med3_f32 v15, v22, s56, v212
	v_med3_f32 v17, v23, s56, v212
	v_mov_b32_e32 v22, 0
	v_med3_f32 v11, v25, s56, v212
	v_cvt_pk_fp8_f32 v22, v15, v17
	v_cvt_pk_fp8_f32 v21, v10, v11 op_sel:[0,0,1]
	v_pk_fma_f32 v[10:11], v[56:57], v[100:101], v[8:9]
	v_pk_fma_f32 v[26:27], v[50:51], v[98:99], v[2:3]
	v_pk_mul_f32 v[10:11], v[18:19], v[10:11] op_sel_hi:[0,1]
	v_pk_mul_f32 v[26:27], v[18:19], v[26:27] op_sel_hi:[0,1]
	v_med3_f32 v10, v10, s56, v212
	v_med3_f32 v11, v11, s56, v212
	v_cvt_pk_fp8_f32 v22, v10, v11 op_sel:[0,0,1]
	v_med3_f32 v10, v26, s56, v212
	v_med3_f32 v11, v27, s56, v212
	v_mov_b32_e32 v23, 0
	v_cvt_pk_fp8_f32 v23, v10, v11
	v_pk_fma_f32 v[24:25], v[52:53], v[32:33], v[4:5]
	v_permlane16_swap_b32_e32 v20, v22
	v_pk_mul_f32 v[18:19], v[18:19], v[24:25] op_sel_hi:[0,1]
	v_med3_f32 v10, v18, s56, v212
	v_med3_f32 v11, v19, s56, v212
	v_cvt_pk_fp8_f32 v23, v10, v11 op_sel:[0,0,1]
	v_pk_fma_f32 v[10:11], v[48:49], v[100:101], v[8:9]
	v_pk_fma_f32 v[8:9], v[40:41], v[100:101], v[8:9]
	v_pk_mul_f32 v[18:19], v[16:17], v[10:11] op_sel_hi:[0,1]
	v_permlane16_swap_b32_e32 v21, v23
	global_store_dwordx4 v[12:13], v[20:23], off offset:128
	v_pk_fma_f32 v[12:13], v[46:47], v[102:103], v[6:7]
	v_pk_fma_f32 v[10:11], v[44:45], v[32:33], v[4:5]
	v_pk_mul_f32 v[12:13], v[16:17], v[12:13] op_sel_hi:[0,1]
	v_pk_fma_f32 v[20:21], v[42:43], v[98:99], v[2:3]
	v_pk_fma_f32 v[6:7], v[38:39], v[102:103], v[6:7]
	v_pk_mul_f32 v[20:21], v[16:17], v[20:21] op_sel_hi:[0,1]
	v_pk_mul_f32 v[16:17], v[16:17], v[10:11] op_sel_hi:[0,1]
	v_med3_f32 v11, v12, s56, v212
	v_med3_f32 v12, v13, s56, v212
	v_mov_b32_e32 v10, 0
	v_cvt_pk_fp8_f32 v10, v11, v12
	v_med3_f32 v11, v18, s56, v212
	v_med3_f32 v12, v19, s56, v212
	v_med3_f32 v13, v21, s56, v212
	v_cvt_pk_fp8_f32 v10, v11, v12 op_sel:[0,0,1]
	v_med3_f32 v12, v20, s56, v212
	v_mov_b32_e32 v11, 0
	v_cvt_pk_fp8_f32 v11, v12, v13
	v_pk_fma_f32 v[2:3], v[34:35], v[98:99], v[2:3]
	v_med3_f32 v12, v16, s56, v212
	v_med3_f32 v13, v17, s56, v212
	v_pk_mul_f32 v[6:7], v[14:15], v[6:7] op_sel_hi:[0,1]
	v_pk_mul_f32 v[2:3], v[14:15], v[2:3] op_sel_hi:[0,1]
	v_cvt_pk_fp8_f32 v11, v12, v13 op_sel:[0,0,1]
	v_med3_f32 v6, v6, s56, v212
	v_med3_f32 v7, v7, s56, v212
	v_mov_b32_e32 v12, 0
	v_med3_f32 v2, v2, s56, v212
	v_med3_f32 v3, v3, s56, v212
	v_mov_b32_e32 v13, 0
	v_cvt_pk_fp8_f32 v12, v6, v7
	v_cvt_pk_fp8_f32 v13, v2, v3
	v_pk_fma_f32 v[4:5], v[36:37], v[32:33], v[4:5]
	v_pk_mul_f32 v[8:9], v[14:15], v[8:9] op_sel_hi:[0,1]
	v_pk_mul_f32 v[4:5], v[14:15], v[4:5] op_sel_hi:[0,1]
	v_med3_f32 v6, v8, s56, v212
	v_med3_f32 v7, v9, s56, v212
	v_med3_f32 v2, v4, s56, v212
	v_med3_f32 v3, v5, s56, v212
	v_cvt_pk_fp8_f32 v12, v6, v7 op_sel:[0,0,1]
	v_cvt_pk_fp8_f32 v13, v2, v3 op_sel:[0,0,1]
	v_permlane16_swap_b32_e32 v91, v93
	v_permlane16_swap_b32_e32 v10, v12
	v_permlane16_swap_b32_e32 v11, v13
	global_store_dwordx4 v[146:147], v[90:93], off offset:128
	global_store_dwordx4 v[30:31], v[10:13], off offset:128
	s_cbranch_vccnz .LBB0_581
	s_andn2_b64 vcc, exec, s[2:3]
	s_cbranch_vccnz .LBB0_580
	s_barrier
	s_branch .LBB0_580
